# W1 conversion loops software-pipelined: next item's 8 global loads issued (into a second register set) before the current item's LDS transpose and fp8 pack
# baseline (speedup 1.0000x reference)
; #define LAS __attribute__((address_space(3)))
; DI void transpose_item(const float* W, int K, int N, bf16_t* WT, int mode, LAS float* scr, int item, int lane) {
;     const int nblk = N / 32, kb = item / nblk, nb = item % nblk, k0 = 64 * kb, n0 = 32 * nb;
;     { const int rr = lane >> 3, c4 = lane & 7; f32x4 v[8];
; #pragma unroll
;       for (int i = 0; i < 8; ++i) v[i] = *(const f32x4*)(W + (size_t)(k0 + 8 * i + rr) * N + n0 + 4 * c4);
; DI void phase_expert_weights(const Frame& F, int l, int which) {
;     ...
;     if (which == 0) {
;         constexpr int IPM = (D / 64) * (2048 / 32);
;         for (int it = F.gw; it < NE * IPM; it += F.NGW) { const int mtx = l * NE + it / IPM, r = it % IPM;
;             transpose_item(F.ap->in[32] + (size_t)mtx * D * 2048, D, 2048, (bf16_t*)(ws + WS_W1 + (size_t)mtx * 2048 * D), 3, scr, r, F.lane); }
.Lpre_1107:
	s_ashr_i32 s7, s7, 6
	s_lshl_b32 s6, s6, 3
	s_add_i32 s6, s6, s7
	s_cmpk_gt_i32 s6, 0x7fff
	s_cbranch_scc1 .Lpre_done
	s_load_dwordx2 s[8:9], s[4:5], 0x128
	s_load_dwordx2 s[36:37], s[4:5], 0x100
	s_lshl_b32 s4, s2, 3
	s_lshl_b32 s2, s7, 14
	s_add_i32 s2, s2, 0
	v_bfe_u32 v30, v0, 3, 3
	v_and_b32_e32 v1, 7, v0
	v_lshlrev_b32_e32 v0, 4, v0
	s_waitcnt lgkmcnt(0)
	s_add_u32 s5, s8, 0x4000000
	v_lshlrev_b32_e32 v2, 2, v1
	v_lshl_add_u32 v3, v1, 4, s2
	v_mul_u32_u24_e32 v4, 0x84, v30
	v_lshlrev_b32_e32 v28, 3, v1
	v_mul_u32_u24_e32 v1, 0x420, v1
	v_and_b32_e32 v34, 0x80, v0
	v_lshlrev_b32_e32 v0, 2, v30
	s_addc_u32 s7, s9, 0
	v_or_b32_e32 v31, 8, v30
	v_or_b32_e32 v32, 16, v30
	v_or_b32_e32 v33, 24, v30
	v_mov_b32_e32 v29, v193
	v_add3_u32 v35, s2, v1, v0
	v_lshlrev_b32_e32 v192, 2, v2
	v_add_u32_e32 v36, v3, v4
	s_ashr_i32 s2, s6, 31
	s_lshr_b32 s2, s2, 22
	s_add_i32 s2, s6, s2
	s_ashr_i32 s8, s2, 10
	s_add_i32 s8, s8, s28
	s_and_b32 s2, s2, 0xfc00
	s_ashr_i32 s9, s8, 31
	s_sub_i32 s2, s6, s2
	s_lshl_b64 s[12:13], s[8:9], 23
	s_add_u32 s17, s36, s12
	s_addc_u32 s19, s37, s13
	s_lshl_b64 s[8:9], s[8:9], 21
	s_add_u32 s8, s5, s8
	s_sext_i32_i16 s10, s2
	s_addc_u32 s9, s7, s9
	s_bfe_u32 s10, s10, 0x60019
	s_add_i32 s10, s2, s10
	s_sext_i32_i16 s12, s10
	s_and_b32 s10, s10, 0xffc0
	s_sub_i32 s2, s2, s10
	s_sext_i32_i16 s2, s2
	s_lshl_b32 s38, s2, 5
	s_ashr_i32 s39, s38, 31
	s_and_b32 s10, s12, 0xffffffc0
	s_lshl_b64 s[12:13], s[38:39], 2
	v_or_b32_e32 v182, s10, v30
	s_add_u32 s12, s17, s12
	s_addc_u32 s13, s19, s13
	v_ashrrev_i32_e32 v183, 31, v182
	v_lshl_add_u64 v[184:185], s[12:13], 0, v[192:193]
	v_lshlrev_b64 v[186:187], 13, v[182:183]
	v_lshl_add_u64 v[186:187], v[184:185], 0, v[186:187]
	global_load_dwordx4 v[150:153], v[186:187], off
	v_or_b32_e32 v186, 8, v182
	v_ashrrev_i32_e32 v187, 31, v186
	v_lshlrev_b64 v[186:187], 13, v[186:187]
	v_lshl_add_u64 v[186:187], v[184:185], 0, v[186:187]
	global_load_dwordx4 v[154:157], v[186:187], off
	v_or_b32_e32 v186, 16, v182
	v_ashrrev_i32_e32 v187, 31, v186
	v_lshlrev_b64 v[186:187], 13, v[186:187]
	v_lshl_add_u64 v[186:187], v[184:185], 0, v[186:187]
	global_load_dwordx4 v[158:161], v[186:187], off
	v_or_b32_e32 v186, 24, v182
	v_ashrrev_i32_e32 v187, 31, v186
	v_lshlrev_b64 v[186:187], 13, v[186:187]
	v_lshl_add_u64 v[186:187], v[184:185], 0, v[186:187]
	global_load_dwordx4 v[162:165], v[186:187], off
	v_or_b32_e32 v186, 32, v182
	v_ashrrev_i32_e32 v187, 31, v186
	v_lshlrev_b64 v[186:187], 13, v[186:187]
	v_lshl_add_u64 v[186:187], v[184:185], 0, v[186:187]
	global_load_dwordx4 v[166:169], v[186:187], off
	v_or_b32_e32 v186, 40, v182
	v_ashrrev_i32_e32 v187, 31, v186
	v_lshlrev_b64 v[186:187], 13, v[186:187]
	v_lshl_add_u64 v[186:187], v[184:185], 0, v[186:187]
	global_load_dwordx4 v[170:173], v[186:187], off
	v_or_b32_e32 v186, 48, v182
	v_ashrrev_i32_e32 v187, 31, v186
	v_lshlrev_b64 v[186:187], 13, v[186:187]
	v_or_b32_e32 v182, 56, v182
	v_lshl_add_u64 v[186:187], v[184:185], 0, v[186:187]
	v_ashrrev_i32_e32 v183, 31, v182
	global_load_dwordx4 v[174:177], v[186:187], off
	v_lshlrev_b64 v[182:183], 13, v[182:183]
	v_lshl_add_u64 v[182:183], v[184:185], 0, v[182:183]
	global_load_dwordx4 v[178:181], v[182:183], off
	s_waitcnt vmcnt(0)
.Lpre_1109:
	s_waitcnt vmcnt(4)
	v_mov_b32_e32 v38, v150
	v_mov_b32_e32 v39, v151
	v_mov_b32_e32 v40, v152
	v_mov_b32_e32 v41, v153
	v_mov_b32_e32 v24, v154
	v_mov_b32_e32 v25, v155
	v_mov_b32_e32 v26, v156
	v_mov_b32_e32 v27, v157
	v_mov_b32_e32 v20, v158
	v_mov_b32_e32 v21, v159
	v_mov_b32_e32 v22, v160
	v_mov_b32_e32 v23, v161
	v_mov_b32_e32 v16, v162
	v_mov_b32_e32 v17, v163
	v_mov_b32_e32 v18, v164
	v_mov_b32_e32 v19, v165
	v_mov_b32_e32 v12, v166
	v_mov_b32_e32 v13, v167
	v_mov_b32_e32 v14, v168
	v_mov_b32_e32 v15, v169
	v_mov_b32_e32 v8, v170
	v_mov_b32_e32 v9, v171
	v_mov_b32_e32 v10, v172
	v_mov_b32_e32 v11, v173
	v_mov_b32_e32 v4, v174
	v_mov_b32_e32 v5, v175
	v_mov_b32_e32 v6, v176
	v_mov_b32_e32 v7, v177
	v_mov_b32_e32 v0, v178
	v_mov_b32_e32 v1, v179
	v_mov_b32_e32 v2, v180
	v_mov_b32_e32 v3, v181
	v_add_u32_e32 v37, 0x420, v36
	s_ashr_i32 s2, s10, 31
	s_add_u32 s54, s8, s10
	s_addc_u32 s55, s9, s2
	s_and_b32 s53, s38, 0xffffff00
	s_mov_b32 s56, s38
	s_add_i32 s6, s6, s4
	s_cmp_lt_i32 s6, 0x8000
	s_cbranch_scc0 .Lcpfp_1109_nopf
	s_ashr_i32 s2, s6, 31
	s_lshr_b32 s2, s2, 22
	s_add_i32 s2, s6, s2
	s_ashr_i32 s8, s2, 10
	s_add_i32 s8, s8, s28
	s_and_b32 s2, s2, 0xfc00
	s_ashr_i32 s9, s8, 31
	s_sub_i32 s2, s6, s2
	s_lshl_b64 s[12:13], s[8:9], 23
	s_add_u32 s17, s36, s12
	s_addc_u32 s19, s37, s13
	s_lshl_b64 s[8:9], s[8:9], 21
	s_add_u32 s8, s5, s8
	s_sext_i32_i16 s10, s2
	s_addc_u32 s9, s7, s9
	s_bfe_u32 s10, s10, 0x60019
	s_add_i32 s10, s2, s10
	s_sext_i32_i16 s12, s10
	s_and_b32 s10, s10, 0xffc0
	s_sub_i32 s2, s2, s10
	s_sext_i32_i16 s2, s2
	s_lshl_b32 s38, s2, 5
	s_ashr_i32 s39, s38, 31
	s_and_b32 s10, s12, 0xffffffc0
	s_lshl_b64 s[12:13], s[38:39], 2
	v_or_b32_e32 v182, s10, v30
	s_add_u32 s12, s17, s12
	s_addc_u32 s13, s19, s13
	v_ashrrev_i32_e32 v183, 31, v182
	v_lshl_add_u64 v[184:185], s[12:13], 0, v[192:193]
	v_lshlrev_b64 v[186:187], 13, v[182:183]
	v_lshl_add_u64 v[186:187], v[184:185], 0, v[186:187]
	global_load_dwordx4 v[150:153], v[186:187], off
	v_or_b32_e32 v186, 8, v182
	v_ashrrev_i32_e32 v187, 31, v186
	v_lshlrev_b64 v[186:187], 13, v[186:187]
	v_lshl_add_u64 v[186:187], v[184:185], 0, v[186:187]
	global_load_dwordx4 v[154:157], v[186:187], off
	v_or_b32_e32 v186, 16, v182
	v_ashrrev_i32_e32 v187, 31, v186
	v_lshlrev_b64 v[186:187], 13, v[186:187]
	v_lshl_add_u64 v[186:187], v[184:185], 0, v[186:187]
	global_load_dwordx4 v[158:161], v[186:187], off
	v_or_b32_e32 v186, 24, v182
	v_ashrrev_i32_e32 v187, 31, v186
	v_lshlrev_b64 v[186:187], 13, v[186:187]
	v_lshl_add_u64 v[186:187], v[184:185], 0, v[186:187]
	global_load_dwordx4 v[162:165], v[186:187], off
	v_or_b32_e32 v186, 32, v182
	v_ashrrev_i32_e32 v187, 31, v186
	v_lshlrev_b64 v[186:187], 13, v[186:187]
	v_lshl_add_u64 v[186:187], v[184:185], 0, v[186:187]
	global_load_dwordx4 v[166:169], v[186:187], off
	v_or_b32_e32 v186, 40, v182
	v_ashrrev_i32_e32 v187, 31, v186
	v_lshlrev_b64 v[186:187], 13, v[186:187]
	v_lshl_add_u64 v[186:187], v[184:185], 0, v[186:187]
	global_load_dwordx4 v[170:173], v[186:187], off
	v_or_b32_e32 v186, 48, v182
	v_ashrrev_i32_e32 v187, 31, v186
	v_lshlrev_b64 v[186:187], 13, v[186:187]
	v_or_b32_e32 v182, 56, v182
	v_lshl_add_u64 v[186:187], v[184:185], 0, v[186:187]
	v_ashrrev_i32_e32 v183, 31, v182
	global_load_dwordx4 v[174:177], v[186:187], off
	v_lshlrev_b64 v[182:183], 13, v[182:183]
	v_lshl_add_u64 v[182:183], v[184:185], 0, v[182:183]
	global_load_dwordx4 v[178:181], v[182:183], off
; #define LAS __attribute__((address_space(3)))
; DI unsigned pk2(float lo, float hi) { return f2bf(lo) | (f2bf(hi) << 16); }
; DI unsigned pk_fp8x4(float a, float b, float c, float d) { int p = 0; p = __builtin_amdgcn_cvt_pk_fp8_f32(a, b, p, false); p = __builtin_amdgcn_cvt_pk_fp8_f32(c, d, p, true); return (unsigned)p; }
; #define LDS_WAIT() asm volatile("s_waitcnt lgkmcnt(0)" ::: "memory")
; DI void transpose_item(const float* W, int K, int N, bf16_t* WT, int mode, LAS float* scr, int item, int lane) {
;     ...
; #pragma unroll
;       for (int i = 0; i < 8; ++i) { LAS float* d = scr + (8 * i + rr) * 33 + 4 * c4; d[0] = v[i].x; d[1] = v[i].y; d[2] = v[i].z; d[3] = v[i].w; } }
;     LDS_WAIT(); asm volatile("" ::: "memory");
;     const int c = lane & 7;
; #pragma unroll
;     for (int j = 0; j < 4; ++j) { const int n = (lane >> 3) + 8 * j; const LAS float* s = scr + (8 * c) * 33 + n;
;         const int row = (mode & 1) ? w1_row(n0 + n) : (n0 + n);
;         if (mode & 2) { u32x2 o; o.x = pk_fp8x4(s[0 * 33] * W8_SCALE, s[1 * 33] * W8_SCALE, s[2 * 33] * W8_SCALE, s[3 * 33] * W8_SCALE); o.y = pk_fp8x4(s[4 * 33] * W8_SCALE, s[5 * 33] * W8_SCALE, s[6 * 33] * W8_SCALE, s[7 * 33] * W8_SCALE);
;             *(u32x2*)((unsigned char*)WT + (size_t)row * K + k0 + 8 * c) = o; }
;         else { u32x4 o; o.x = pk2(s[0 * 33], s[1 * 33]); o.y = pk2(s[2 * 33], s[3 * 33]); o.z = pk2(s[4 * 33], s[5 * 33]); o.w = pk2(s[6 * 33], s[7 * 33]);
;             *(u32x4*)(WT + (size_t)row * K + k0 + 8 * c) = o; } }
.Lcpfp_1109_nopf:
	ds_write2_b32 v36, v38, v39 offset1:1
	ds_write2_b32 v36, v40, v41 offset0:2 offset1:3
	ds_write2_b32 v37, v24, v25 offset1:1
	v_add_u32_e32 v24, 0x428, v36
	ds_write2_b32 v24, v26, v27 offset1:1
	v_add_u32_e32 v24, 0x840, v36
	ds_write2_b32 v24, v20, v21 offset1:1
	v_add_u32_e32 v20, 0x848, v36
	ds_write2_b32 v20, v22, v23 offset1:1
	v_add_u32_e32 v20, 0xc60, v36
	ds_write2_b32 v20, v16, v17 offset1:1
	v_add_u32_e32 v16, 0xc68, v36
	ds_write2_b32 v16, v18, v19 offset1:1
	v_add_u32_e32 v16, 0x1080, v36
	ds_write2_b32 v16, v12, v13 offset1:1
	v_add_u32_e32 v12, 0x1088, v36
	ds_write2_b32 v12, v14, v15 offset1:1
	v_add_u32_e32 v12, 0x14a0, v36
	v_mov_b32_e32 v13, v193
	ds_write2_b32 v12, v8, v9 offset1:1
	v_add_u32_e32 v8, 0x14a8, v36
	ds_write2_b32 v8, v10, v11 offset1:1
	v_add_u32_e32 v8, 0x18c0, v36
	v_mov_b32_e32 v12, v193
	ds_write2_b32 v8, v4, v5 offset1:1
	v_add_u32_e32 v4, 0x18c8, v36
	ds_write2_b32 v4, v6, v7 offset1:1
	v_add_u32_e32 v4, 0x1ce0, v36
	ds_write2_b32 v4, v0, v1 offset1:1
	v_add_u32_e32 v0, 0x1ce8, v36
	ds_write2_b32 v0, v2, v3 offset1:1
	s_waitcnt lgkmcnt(0)
	ds_read2_b32 v[4:5], v35 offset1:8
	ds_read2_b32 v[6:7], v35 offset0:33 offset1:41
	ds_read2_b32 v[14:15], v35 offset0:132 offset1:140
	ds_read2_b32 v[16:17], v35 offset0:165 offset1:173
	ds_read2_b32 v[8:9], v35 offset0:66 offset1:74
	ds_read2_b32 v[10:11], v35 offset0:99 offset1:107
	s_waitcnt lgkmcnt(5)
	v_mul_f32_e32 v3, 0x42800000, v4
	s_waitcnt lgkmcnt(4)
	v_mul_f32_e32 v4, 0x42800000, v6
	ds_read2_b32 v[18:19], v35 offset0:198 offset1:206
	ds_read2_b32 v[20:21], v35 offset0:231 offset1:239
	v_cvt_pk_fp8_f32 v12, v3, v4
	s_waitcnt lgkmcnt(5)
	v_mul_f32_e32 v3, 0x42800000, v14
	s_waitcnt lgkmcnt(4)
	v_mul_f32_e32 v4, 0x42800000, v16
	v_cvt_pk_fp8_f32 v13, v3, v4
	v_or_b32_e32 v2, s56, v30
	v_lshrrev_b32_e32 v2, 1, v2
	s_waitcnt lgkmcnt(3)
	v_mul_f32_e32 v6, 0x42800000, v8
	s_waitcnt lgkmcnt(2)
	v_mul_f32_e32 v8, 0x42800000, v10
	v_and_b32_e32 v2, 0x73, v2
	v_cvt_pk_fp8_f32 v12, v6, v8 op_sel:[0,0,1]
	s_waitcnt lgkmcnt(1)
	v_mul_f32_e32 v6, 0x42800000, v18
	s_waitcnt lgkmcnt(0)
	v_mul_f32_e32 v8, 0x42800000, v20
	v_or3_b32 v2, s53, v2, v34
	v_cvt_pk_fp8_f32 v13, v6, v8 op_sel:[0,0,1]
	v_ashrrev_i32_e32 v3, 31, v2
	v_lshl_add_u64 v[0:1], s[54:55], 0, v[28:29]
	v_lshlrev_b64 v[2:3], 10, v[2:3]
	v_lshl_add_u64 v[2:3], v[0:1], 0, v[2:3]
	global_store_dwordx2 v[2:3], v[12:13], off
	v_mul_f32_e32 v3, 0x42800000, v5
	v_mul_f32_e32 v5, 0x42800000, v7
	v_mov_b32_e32 v4, v193
	v_cvt_pk_fp8_f32 v4, v3, v5
	v_mul_f32_e32 v6, 0x42800000, v9
	v_mul_f32_e32 v7, 0x42800000, v11
	v_mul_f32_e32 v3, 0x42800000, v15
	v_cvt_pk_fp8_f32 v4, v6, v7 op_sel:[0,0,1]
	v_mul_f32_e32 v6, 0x42800000, v17
	v_mov_b32_e32 v5, v193
	v_cvt_pk_fp8_f32 v5, v3, v6
	v_or_b32_e32 v2, s56, v31
	v_lshrrev_b32_e32 v2, 1, v2
	v_and_b32_e32 v2, 0x77, v2
	v_mul_f32_e32 v7, 0x42800000, v19
	v_mul_f32_e32 v8, 0x42800000, v21
	v_or3_b32 v2, s53, v2, v34
	v_cvt_pk_fp8_f32 v5, v7, v8 op_sel:[0,0,1]
	v_ashrrev_i32_e32 v3, 31, v2
	v_lshlrev_b64 v[2:3], 10, v[2:3]
	v_lshl_add_u64 v[2:3], v[0:1], 0, v[2:3]
	global_store_dwordx2 v[2:3], v[4:5], off
	ds_read2_b32 v[4:5], v35 offset0:16 offset1:24
	ds_read2_b32 v[6:7], v35 offset0:49 offset1:57
	ds_read2_b32 v[14:15], v35 offset0:148 offset1:156
	ds_read2_b32 v[16:17], v35 offset0:181 offset1:189
	ds_read2_b32 v[8:9], v35 offset0:82 offset1:90
	ds_read2_b32 v[10:11], v35 offset0:115 offset1:123
	s_waitcnt lgkmcnt(5)
	v_mul_f32_e32 v3, 0x42800000, v4
	s_waitcnt lgkmcnt(4)
	v_mul_f32_e32 v4, 0x42800000, v6
	v_mov_b32_e32 v12, v193
	ds_read2_b32 v[18:19], v35 offset0:214 offset1:222
	ds_read2_b32 v[20:21], v35 offset0:247 offset1:255
	v_cvt_pk_fp8_f32 v12, v3, v4
	s_waitcnt lgkmcnt(5)
	v_mul_f32_e32 v3, 0x42800000, v14
	s_waitcnt lgkmcnt(4)
	v_mul_f32_e32 v4, 0x42800000, v16
	v_mov_b32_e32 v13, v193
	v_cvt_pk_fp8_f32 v13, v3, v4
	v_or_b32_e32 v2, s56, v32
	v_lshrrev_b32_e32 v2, 1, v2
	s_waitcnt lgkmcnt(3)
	v_mul_f32_e32 v6, 0x42800000, v8
	s_waitcnt lgkmcnt(2)
	v_mul_f32_e32 v8, 0x42800000, v10
	v_and_b32_e32 v2, 0x7b, v2
	v_cvt_pk_fp8_f32 v12, v6, v8 op_sel:[0,0,1]
	s_waitcnt lgkmcnt(1)
	v_mul_f32_e32 v6, 0x42800000, v18
	s_waitcnt lgkmcnt(0)
	v_mul_f32_e32 v8, 0x42800000, v20
	v_or3_b32 v2, s53, v2, v34
	v_cvt_pk_fp8_f32 v13, v6, v8 op_sel:[0,0,1]
	v_ashrrev_i32_e32 v3, 31, v2
	v_lshlrev_b64 v[2:3], 10, v[2:3]
	v_lshl_add_u64 v[2:3], v[0:1], 0, v[2:3]
	global_store_dwordx2 v[2:3], v[12:13], off
	v_or_b32_e32 v2, s56, v33
	v_bfe_u32 v2, v2, 1, 7
	v_or3_b32 v4, s53, v2, v34
	v_mul_f32_e32 v3, 0x42800000, v5
	v_mul_f32_e32 v5, 0x42800000, v7
	v_mov_b32_e32 v2, v193
	v_cvt_pk_fp8_f32 v2, v3, v5
	v_mul_f32_e32 v6, 0x42800000, v9
	v_mul_f32_e32 v7, 0x42800000, v11
	v_mul_f32_e32 v5, 0x42800000, v15
	v_cvt_pk_fp8_f32 v2, v6, v7 op_sel:[0,0,1]
	v_mul_f32_e32 v6, 0x42800000, v17
	v_mov_b32_e32 v3, v193
	v_cvt_pk_fp8_f32 v3, v5, v6
	v_mul_f32_e32 v7, 0x42800000, v19
	v_mul_f32_e32 v8, 0x42800000, v21
	v_ashrrev_i32_e32 v5, 31, v4
	v_cvt_pk_fp8_f32 v3, v7, v8 op_sel:[0,0,1]
	v_lshlrev_b64 v[4:5], 10, v[4:5]
	v_lshl_add_u64 v[0:1], v[0:1], 0, v[4:5]
	global_store_dwordx2 v[0:1], v[2:3], off
	s_waitcnt lgkmcnt(0)
	s_cmp_lt_i32 s6, 0x8000
	s_cbranch_scc1 .Lpre_1109
